# baseline (speedup 1.0000x reference)
_Z9gemm_gldsILi256ELi192ELi4ELi2ELi2ELi4ELi8ELi0ELi4096ELi3072ELi1024EEvPKDF16_S1_PfPKfS4_PKiPDF16_S7_S7_:
	s_ashr_i32 s3, s2, 3
	s_lshr_b32 s9, s3, 30
	s_add_i32 s9, s3, s9
	s_lshl_b32 s8, s2, 1
	s_ashr_i32 s10, s9, 2
	s_and_b32 s9, s9, 0xfffffc
	s_lshl_b32 s2, s2, 3
	s_load_dwordx4 s[4:7], s[0:1], 0x0
	s_and_b32 s8, s8, 12
	s_sub_i32 s3, s3, s9
	s_and_b32 s20, s2, 8
	s_add_i32 s8, s8, s3
	s_add_i32 s20, s20, s10
	s_lshl_b32 s16, s8, 8
	s_mul_i32 s2, s20, 0xc0
	v_lshlrev_b32_e32 v139, 4, v0
	v_and_b32_e32 v1, 32, v0
	s_ashr_i32 s17, s16, 31
	s_ashr_i32 s3, s2, 31
	v_lshrrev_b32_e32 v2, 3, v0
	v_bfe_u32 v46, v0, 2, 4
	v_bitop3_b32 v1, v139, v1, 48 bitop3:0x6c
	s_lshl_b64 s[8:9], s[16:17], 11
	s_lshl_b64 s[10:11], s[2:3], 11
	v_and_or_b32 v2, v2, 48, v46
	v_and_or_b32 v47, v0, 64, v1
	s_waitcnt lgkmcnt(0)
	s_add_u32 s2, s4, s8
	s_addc_u32 s3, s5, s9
	v_lshl_or_b32 v2, v2, 11, v47
	v_add_u32_e32 v194, 0x100, v2
	v_mov_b32_e32 v3, 0
	v_readfirstlane_b32 s4, v139
	v_or_b32_e32 v1, 0x2000, v139
	s_add_u32 s18, s6, s10
	v_lshl_add_u64 v[4:5], s[2:3], 0, v[2:3]
	s_mov_b32 m0, s4
	s_mov_b64 s[4:5], 0x20000
	v_readfirstlane_b32 s6, v1
	v_or_b32_e32 v1, 0x4000, v139
	s_addc_u32 s19, s7, s11
	v_readfirstlane_b32 s45, v139
	s_mov_b64 s[24:25], s[2:3]
	s_add_u32 s26, s2, 0x20000
	s_addc_u32 s27, s3, 0
	s_add_u32 s28, s2, 0x40000
	s_addc_u32 s29, s3, 0
	s_add_u32 s30, s2, 0x60000
	s_addc_u32 s31, s3, 0
	s_mov_b64 s[32:33], s[18:19]
	s_add_u32 s34, s18, 0x20000
	s_addc_u32 s35, s19, 0
	s_add_u32 s36, s18, 0x40000
	s_addc_u32 s37, s19, 0
	global_load_lds_dwordx4 v2, s[2:3]
	v_lshl_add_u64 v[8:9], v[4:5], 0, s[4:5]
	s_mov_b32 m0, s6
	s_mov_b64 s[6:7], 0x40000
	v_readfirstlane_b32 s8, v1
	global_load_lds_dwordx4 v[8:9], off
	v_lshl_add_u64 v[8:9], v[4:5], 0, s[6:7]
	s_mov_b32 m0, s8
	s_mov_b64 s[8:9], 0x60000
	v_or_b32_e32 v1, 0x6000, v139
	global_load_lds_dwordx4 v[8:9], off
	v_lshl_add_u64 v[8:9], v[4:5], 0, s[8:9]
	v_readfirstlane_b32 s8, v1
	v_or_b32_e32 v1, 0x8000, v139
	v_lshl_add_u64 v[6:7], s[18:19], 0, v[2:3]
	s_mov_b32 m0, s8
	v_readfirstlane_b32 s8, v1
	v_or_b32_e32 v1, 0xa000, v139
	global_load_lds_dwordx4 v[8:9], off
	s_mov_b32 m0, s8
	v_lshl_add_u64 v[8:9], v[6:7], 0, s[4:5]
	v_readfirstlane_b32 s4, v1
	v_or_b32_e32 v1, 0xc000, v139
	global_load_lds_dwordx4 v2, s[18:19]
	s_mov_b32 m0, s4
	v_readfirstlane_b32 s4, v1
	v_or_b32_e32 v1, 0xe000, v139
	global_load_lds_dwordx4 v[8:9], off
	v_lshl_add_u64 v[8:9], v[6:7], 0, s[6:7]
	s_mov_b32 m0, s4
	s_mov_b64 s[4:5], 0x80
	v_readfirstlane_b32 s6, v1
	v_or_b32_e32 v1, 0x10000, v139
	global_load_lds_dwordx4 v[8:9], off
	v_lshl_add_u64 v[8:9], v[4:5], 0, s[4:5]
	s_mov_b32 m0, s6
	s_mov_b64 s[6:7], 0x20080
	v_readfirstlane_b32 s8, v1
	v_or_b32_e32 v1, 0x12000, v139
	global_load_lds_dwordx4 v[8:9], off
	v_lshl_add_u64 v[8:9], v[4:5], 0, s[6:7]
	s_mov_b32 m0, s8
	v_readfirstlane_b32 s10, v1
	global_load_lds_dwordx4 v[8:9], off
	s_mov_b64 s[8:9], 0x40080
	s_mov_b32 m0, s10
	s_mov_b64 s[10:11], 0x60080
	v_or_b32_e32 v1, 0x14000, v139
	v_lshl_add_u64 v[8:9], v[4:5], 0, s[8:9]
	v_lshl_add_u64 v[4:5], v[4:5], 0, s[10:11]
	v_readfirstlane_b32 s10, v1
	global_load_lds_dwordx4 v[8:9], off
	s_mov_b32 m0, s10
	v_or_b32_e32 v1, 0x16000, v139
	global_load_lds_dwordx4 v[4:5], off
	v_lshl_add_u64 v[4:5], v[6:7], 0, s[4:5]
	v_readfirstlane_b32 s4, v1
	v_or_b32_e32 v1, 0x18000, v139
	s_mov_b32 m0, s4
	v_readfirstlane_b32 s4, v1
	v_or_b32_e32 v1, 0x1a000, v139
	global_load_lds_dwordx4 v[4:5], off
	v_lshl_add_u64 v[4:5], v[6:7], 0, s[6:7]
	s_mov_b32 m0, s4
	v_readfirstlane_b32 s4, v1
	global_load_lds_dwordx4 v[4:5], off
	v_lshl_add_u64 v[4:5], v[6:7], 0, s[8:9]
	s_mov_b32 m0, s4
	v_lshrrev_b32_e32 v2, 7, v0
	global_load_lds_dwordx4 v[4:5], off
	s_load_dwordx4 s[12:15], s[0:1], 0x38
	s_load_dwordx8 s[4:11], s[0:1], 0x18
	v_lshlrev_b32_e32 v4, 6, v0
	v_and_b32_e32 v138, 48, v0
	v_and_b32_e32 v4, 0x3c0, v4
	v_lshlrev_b32_e32 v6, 2, v0
	v_bfe_u32 v144, v0, 6, 1
	v_or_b32_e32 v14, v4, v138
	v_lshlrev_b32_e32 v5, 13, v2
	v_and_b32_e32 v15, 32, v6
	v_and_b32_e32 v1, 15, v0
	v_bitop3_b32 v151, v4, v15, v138 bitop3:0x36
	v_bitop3_b32 v146, v5, v14, v15 bitop3:0xf6
	v_mul_u32_u24_e32 v152, 0x3000, v144
	v_lshl_or_b32 v145, v2, 6, s16
	v_or_b32_e32 v4, v145, v1
	v_ashrrev_i32_e32 v5, 31, v4
	s_waitcnt lgkmcnt(0)
	v_lshl_add_u64 v[4:5], v[4:5], 2, s[8:9]
	global_load_dword v150, v[4:5], off
	global_load_dword v149, v[4:5], off offset:64
	global_load_dword v148, v[4:5], off offset:128
	global_load_dword v147, v[4:5], off offset:192
	v_bitop3_b32 v153, v152, v14, v15 bitop3:0xf6
	v_mov_b32_e32 v48, v3
	v_mov_b32_e32 v49, v3
	v_mov_b32_e32 v50, v3
	v_mov_b32_e32 v51, v3
	v_mov_b32_e32 v52, v3
	v_mov_b32_e32 v53, v3
	v_mov_b32_e32 v54, v3
	v_mov_b32_e32 v55, v3
	v_mov_b32_e32 v56, v3
	v_mov_b32_e32 v57, v3
	v_mov_b32_e32 v58, v3
	v_mov_b32_e32 v59, v3
	v_mov_b32_e32 v60, v3
	v_mov_b32_e32 v61, v3
	v_mov_b32_e32 v62, v3
	v_mov_b32_e32 v63, v3
	v_mov_b32_e32 v64, v3
	v_mov_b32_e32 v65, v3
	v_mov_b32_e32 v66, v3
	v_mov_b32_e32 v67, v3
	v_mov_b32_e32 v68, v3
	v_mov_b32_e32 v69, v3
	v_mov_b32_e32 v70, v3
	v_mov_b32_e32 v71, v3
	v_mov_b32_e32 v72, v3
	v_mov_b32_e32 v73, v3
	v_mov_b32_e32 v74, v3
	v_mov_b32_e32 v75, v3
	v_mov_b32_e32 v76, v3
	v_mov_b32_e32 v77, v3
	v_mov_b32_e32 v86, v3
	v_mov_b32_e32 v87, v3
	v_mov_b32_e32 v88, v3
	v_mov_b32_e32 v89, v3
	v_mov_b32_e32 v98, v3
	v_mov_b32_e32 v99, v3
	v_mov_b32_e32 v100, v3
	v_mov_b32_e32 v101, v3
	v_mov_b32_e32 v130, v3
	v_mov_b32_e32 v131, v3
	v_mov_b32_e32 v132, v3
	v_mov_b32_e32 v133, v3
	v_mov_b32_e32 v78, v3
	v_mov_b32_e32 v79, v3
	v_mov_b32_e32 v80, v3
	v_mov_b32_e32 v81, v3
	v_mov_b32_e32 v82, v3
	v_mov_b32_e32 v83, v3
	v_mov_b32_e32 v84, v3
	v_mov_b32_e32 v85, v3
	v_mov_b32_e32 v90, v3
	v_mov_b32_e32 v91, v3
	v_mov_b32_e32 v92, v3
	v_mov_b32_e32 v93, v3
	v_mov_b32_e32 v94, v3
	v_mov_b32_e32 v95, v3
	v_mov_b32_e32 v96, v3
	v_mov_b32_e32 v97, v3
	v_mov_b32_e32 v102, v3
	v_mov_b32_e32 v103, v3
	v_mov_b32_e32 v104, v3
	v_mov_b32_e32 v105, v3
	v_mov_b32_e32 v106, v3
	v_mov_b32_e32 v107, v3
	v_mov_b32_e32 v108, v3
	v_mov_b32_e32 v109, v3
	v_mov_b32_e32 v110, v3
	v_mov_b32_e32 v111, v3
	v_mov_b32_e32 v112, v3
	v_mov_b32_e32 v113, v3
	v_mov_b32_e32 v114, v3
	v_mov_b32_e32 v115, v3
	v_mov_b32_e32 v116, v3
	v_mov_b32_e32 v117, v3
	v_mov_b32_e32 v118, v3
	v_mov_b32_e32 v119, v3
	v_mov_b32_e32 v120, v3
	v_mov_b32_e32 v121, v3
	v_mov_b32_e32 v122, v3
	v_mov_b32_e32 v123, v3
	v_mov_b32_e32 v124, v3
	v_mov_b32_e32 v125, v3
	v_mov_b32_e32 v134, v3
	v_mov_b32_e32 v135, v3
	v_mov_b32_e32 v136, v3
	v_mov_b32_e32 v137, v3
	v_mov_b32_e32 v126, v3
	v_mov_b32_e32 v127, v3
	v_mov_b32_e32 v128, v3
	v_mov_b32_e32 v129, v3
	s_waitcnt vmcnt(7) lgkmcnt(0)
	s_barrier
	ds_read_b128 v[42:45], v146
	ds_read_b128 v[38:41], v146 offset:2048
	ds_read_b128 v[10:13], v146 offset:4096
	ds_read_b128 v[6:9], v146 offset:6144
	ds_read_b128 v[22:25], v153 offset:32768
	ds_read_b128 v[18:21], v153 offset:34816
	ds_read_b128 v[30:33], v153 offset:36864
	ds_read_b128 v[26:29], v153 offset:38912
	ds_read_b128 v[34:37], v153 offset:40960
	ds_read_b128 v[14:17], v153 offset:43008
	v_lshl_or_b32 v2, v2, 15, v47
	v_lshl_or_b32 v2, v46, 11, v2
	v_lshl_add_u64 v[140:141], s[18:19], 0, v[2:3]
	v_lshl_add_u64 v[142:143], s[2:3], 0, v[2:3]
	s_mov_b32 s21, 0
	s_mov_b64 s[0:1], 0
	s_mov_b64 s[2:3], 0x100
	s_mov_b64 s[8:9], 0x20100
	s_mov_b64 s[16:17], 0x40100
	s_mov_b64 s[18:19], 0x60100
	v_mov_b32_e32 v2, v3
	v_mov_b32_e32 v4, v3
	v_mov_b32_e32 v5, v3
	v_mov_b32_e32 v46, v3
	v_mov_b32_e32 v47, v3
.LBB2_1:
	s_mul_i32 s22, s21, 0xe000
	v_add_u32_e32 v196, s22, v146
	v_add_u32_e32 v197, s22, v153
	s_add_u32 s46, s22, s45
	s_add_i32 s21, s21, 1
	s_waitcnt lgkmcnt(0)
	v_mfma_f32_16x16x32_f16 v[130:133], v[22:25], v[42:45], v[130:133]
	ds_read_b128 v[154:157], v196 offset:1024
	ds_read_b128 v[158:161], v196 offset:3072
	v_mfma_f32_16x16x32_f16 v[98:101], v[18:21], v[42:45], v[98:101]
	ds_read_b128 v[162:165], v196 offset:5120
	ds_read_b128 v[166:169], v196 offset:7168
	v_mfma_f32_16x16x32_f16 v[86:89], v[30:33], v[42:45], v[86:89]
	ds_read_b128 v[170:173], v197 offset:33792
	ds_read_b128 v[174:177], v197 offset:35840
	v_mfma_f32_16x16x32_f16 v[74:77], v[26:29], v[42:45], v[74:77]
	ds_read_b128 v[178:181], v197 offset:37888
	ds_read_b128 v[182:185], v197 offset:39936
	v_mfma_f32_16x16x32_f16 v[70:73], v[42:45], v[34:37], v[70:73]
	ds_read_b128 v[186:189], v197 offset:41984
	ds_read_b128 v[190:193], v197 offset:44032
	v_mfma_f32_16x16x32_f16 v[66:69], v[42:45], v[14:17], v[66:69]
	v_mfma_f32_16x16x32_f16 v[62:65], v[22:25], v[38:41], v[62:65]
	v_mfma_f32_16x16x32_f16 v[58:61], v[18:21], v[38:41], v[58:61]
	v_mfma_f32_16x16x32_f16 v[54:57], v[30:33], v[38:41], v[54:57]
	v_mfma_f32_16x16x32_f16 v[50:53], v[26:29], v[38:41], v[50:53]
	v_mfma_f32_16x16x32_f16 v[46:49], v[38:41], v[34:37], v[46:49]
	v_mfma_f32_16x16x32_f16 v[2:5], v[38:41], v[14:17], v[2:5]
	v_mfma_f32_16x16x32_f16 v[78:81], v[22:25], v[10:13], v[78:81]
	v_mfma_f32_16x16x32_f16 v[82:85], v[18:21], v[10:13], v[82:85]
	v_mfma_f32_16x16x32_f16 v[90:93], v[30:33], v[10:13], v[90:93]
	v_mfma_f32_16x16x32_f16 v[94:97], v[26:29], v[10:13], v[94:97]
	v_mfma_f32_16x16x32_f16 v[102:105], v[10:13], v[34:37], v[102:105]
	v_mfma_f32_16x16x32_f16 v[106:109], v[10:13], v[14:17], v[106:109]
	v_mfma_f32_16x16x32_f16 v[110:113], v[22:25], v[6:9], v[110:113]
	v_mfma_f32_16x16x32_f16 v[114:117], v[18:21], v[6:9], v[114:117]
	v_mfma_f32_16x16x32_f16 v[118:121], v[30:33], v[6:9], v[118:121]
	v_mfma_f32_16x16x32_f16 v[122:125], v[26:29], v[6:9], v[122:125]
	v_mfma_f32_16x16x32_f16 v[134:137], v[6:9], v[34:37], v[134:137]
	v_mfma_f32_16x16x32_f16 v[126:129], v[6:9], v[14:17], v[126:129]
	s_cmp_lg_u32 s21, 2
	s_cselect_b32 s21, s21, 0
	s_mul_i32 s22, s21, 0xe000
	v_add_u32_e32 v196, s22, v146
	v_add_u32_e32 v197, s22, v153
	s_waitcnt vmcnt(0) lgkmcnt(0)
	s_barrier
	s_mov_b32 m0, s46
	s_nop 0
	global_load_lds_dwordx4 v194, s[24:25]
	s_add_u32 m0, s46, 0x2000
	s_nop 0
	global_load_lds_dwordx4 v194, s[26:27]
	s_add_u32 m0, s46, 0x4000
	s_nop 0
	global_load_lds_dwordx4 v194, s[28:29]
	s_add_u32 m0, s46, 0x6000
	s_nop 0
	global_load_lds_dwordx4 v194, s[30:31]
	s_add_u32 m0, s46, 0x8000
	s_nop 0
	global_load_lds_dwordx4 v194, s[32:33]
	s_add_u32 m0, s46, 0xa000
	s_nop 0
	global_load_lds_dwordx4 v194, s[34:35]
	s_add_u32 m0, s46, 0xc000
	s_nop 0
	global_load_lds_dwordx4 v194, s[36:37]
	v_add_u32_e32 v194, 0x80, v194
	v_mfma_f32_16x16x32_f16 v[130:133], v[170:173], v[154:157], v[130:133]
	ds_read_b128 v[42:45], v196
	ds_read_b128 v[38:41], v196 offset:2048
	v_mfma_f32_16x16x32_f16 v[98:101], v[174:177], v[154:157], v[98:101]
	ds_read_b128 v[10:13], v196 offset:4096
	ds_read_b128 v[6:9], v196 offset:6144
	v_mfma_f32_16x16x32_f16 v[86:89], v[178:181], v[154:157], v[86:89]
	ds_read_b128 v[22:25], v197 offset:32768
	ds_read_b128 v[18:21], v197 offset:34816
	v_mfma_f32_16x16x32_f16 v[74:77], v[182:185], v[154:157], v[74:77]
	ds_read_b128 v[30:33], v197 offset:36864
	ds_read_b128 v[26:29], v197 offset:38912
	v_mfma_f32_16x16x32_f16 v[70:73], v[154:157], v[186:189], v[70:73]
	ds_read_b128 v[34:37], v197 offset:40960
	ds_read_b128 v[14:17], v197 offset:43008
	v_mfma_f32_16x16x32_f16 v[66:69], v[154:157], v[190:193], v[66:69]
	v_mfma_f32_16x16x32_f16 v[62:65], v[170:173], v[158:161], v[62:65]
	v_mfma_f32_16x16x32_f16 v[58:61], v[174:177], v[158:161], v[58:61]
	v_mfma_f32_16x16x32_f16 v[54:57], v[178:181], v[158:161], v[54:57]
	v_mfma_f32_16x16x32_f16 v[50:53], v[182:185], v[158:161], v[50:53]
	v_mfma_f32_16x16x32_f16 v[46:49], v[158:161], v[186:189], v[46:49]
	v_mfma_f32_16x16x32_f16 v[2:5], v[158:161], v[190:193], v[2:5]
	v_mfma_f32_16x16x32_f16 v[78:81], v[170:173], v[162:165], v[78:81]
	v_mfma_f32_16x16x32_f16 v[82:85], v[174:177], v[162:165], v[82:85]
	v_mfma_f32_16x16x32_f16 v[90:93], v[178:181], v[162:165], v[90:93]
	v_mfma_f32_16x16x32_f16 v[94:97], v[182:185], v[162:165], v[94:97]
	v_mfma_f32_16x16x32_f16 v[102:105], v[162:165], v[186:189], v[102:105]
	v_mfma_f32_16x16x32_f16 v[106:109], v[162:165], v[190:193], v[106:109]
	v_mfma_f32_16x16x32_f16 v[110:113], v[170:173], v[166:169], v[110:113]
	v_mfma_f32_16x16x32_f16 v[114:117], v[174:177], v[166:169], v[114:117]
	v_mfma_f32_16x16x32_f16 v[118:121], v[178:181], v[166:169], v[118:121]
	v_mfma_f32_16x16x32_f16 v[122:125], v[182:185], v[166:169], v[122:125]
	v_mfma_f32_16x16x32_f16 v[134:137], v[166:169], v[186:189], v[134:137]
	v_mfma_f32_16x16x32_f16 v[126:129], v[166:169], v[190:193], v[126:129]
	s_add_u32 s0, s0, 0x80
	s_addc_u32 s1, s1, 0
	s_cmpk_eq_i32 s0, 0x700
	s_cbranch_scc0 .LBB2_1
	s_waitcnt lgkmcnt(0)
	v_mfma_f32_16x16x32_f16 v[130:133], v[22:25], v[42:45], v[130:133]
	ds_read_b128 v[140:143], v146 offset:1024
	ds_read_b128 v[154:157], v146 offset:3072
	v_mfma_f32_16x16x32_f16 v[98:101], v[18:21], v[42:45], v[98:101]
	ds_read_b128 v[158:161], v146 offset:5120
	ds_read_b128 v[162:165], v146 offset:7168
	v_mfma_f32_16x16x32_f16 v[86:89], v[30:33], v[42:45], v[86:89]
	ds_read_b128 v[166:169], v153 offset:33792
	ds_read_b128 v[170:173], v153 offset:35840
	v_mfma_f32_16x16x32_f16 v[74:77], v[26:29], v[42:45], v[74:77]
	ds_read_b128 v[174:177], v153 offset:37888
	ds_read_b128 v[178:181], v153 offset:39936
	v_mfma_f32_16x16x32_f16 v[70:73], v[42:45], v[34:37], v[70:73]
	ds_read_b128 v[182:185], v153 offset:41984
	ds_read_b128 v[186:189], v153 offset:44032
	v_mfma_f32_16x16x32_f16 v[42:45], v[42:45], v[14:17], v[66:69]
	v_mfma_f32_16x16x32_f16 v[62:65], v[22:25], v[38:41], v[62:65]
	v_mfma_f32_16x16x32_f16 v[58:61], v[18:21], v[38:41], v[58:61]
	v_mfma_f32_16x16x32_f16 v[54:57], v[30:33], v[38:41], v[54:57]
	v_mfma_f32_16x16x32_f16 v[50:53], v[26:29], v[38:41], v[50:53]
	v_mfma_f32_16x16x32_f16 v[46:49], v[38:41], v[34:37], v[46:49]
	v_mfma_f32_16x16x32_f16 v[2:5], v[38:41], v[14:17], v[2:5]
	v_mfma_f32_16x16x32_f16 v[38:41], v[22:25], v[10:13], v[78:81]
	v_mfma_f32_16x16x32_f16 v[66:69], v[18:21], v[10:13], v[82:85]
	v_mfma_f32_16x16x32_f16 v[78:81], v[30:33], v[10:13], v[90:93]
	v_mfma_f32_16x16x32_f16 v[82:85], v[26:29], v[10:13], v[94:97]
	v_mfma_f32_16x16x32_f16 v[90:93], v[10:13], v[34:37], v[102:105]
	v_mfma_f32_16x16x32_f16 v[94:97], v[10:13], v[14:17], v[106:109]
	v_mfma_f32_16x16x32_f16 v[22:25], v[22:25], v[6:9], v[110:113]
	v_mfma_f32_16x16x32_f16 v[102:105], v[18:21], v[6:9], v[114:117]
	v_or_b32_e32 v21, v151, v152
	v_and_b32_e32 v20, 63, v0
	v_mfma_f32_16x16x32_f16 v[30:33], v[30:33], v[6:9], v[118:121]
	v_mfma_f32_16x16x32_f16 v[26:29], v[26:29], v[6:9], v[122:125]
	v_mfma_f32_16x16x32_f16 v[34:37], v[6:9], v[34:37], v[134:137]
	v_mfma_f32_16x16x32_f16 v[6:9], v[6:9], v[14:17], v[126:129]
	v_add_u32_e32 v10, 0x16800, v21
	s_waitcnt vmcnt(0) lgkmcnt(0)
	s_waitcnt lgkmcnt(0)
	v_mfma_f32_16x16x32_f16 v[16:19], v[166:169], v[140:143], v[130:133]
	s_barrier
	ds_read_b128 v[106:109], v146 offset:57344
	ds_read_b128 v[110:113], v146 offset:59392
	v_mfma_f32_16x16x32_f16 v[98:101], v[170:173], v[140:143], v[98:101]
	ds_read_b128 v[114:117], v146 offset:61440
	ds_read_b128 v[12:15], v146 offset:63488
	v_add_u32_e32 v0, 0x16000, v21
	v_mfma_f32_16x16x32_f16 v[86:89], v[174:177], v[140:143], v[86:89]
	ds_read_b128 v[122:125], v10
	v_add_u32_e32 v10, 0x17000, v21
	ds_read_b128 v[118:121], v0
	v_mfma_f32_16x16x32_f16 v[74:77], v[178:181], v[140:143], v[74:77]
	ds_read_b128 v[126:129], v10
	v_add_u32_e32 v10, 0x17800, v21
	ds_read_b128 v[130:133], v10
	v_mfma_f32_16x16x32_f16 v[70:73], v[140:143], v[182:185], v[70:73]
	ds_read_b128 v[134:137], v0 offset:8192
	ds_read_b128 v[190:193], v0 offset:10240
	v_mfma_f32_16x16x32_f16 v[42:45], v[140:143], v[186:189], v[42:45]
	v_mfma_f32_16x16x32_f16 v[62:65], v[166:169], v[154:157], v[62:65]
	v_mfma_f32_16x16x32_f16 v[58:61], v[170:173], v[154:157], v[58:61]
	v_mfma_f32_16x16x32_f16 v[54:57], v[174:177], v[154:157], v[54:57]
	v_mfma_f32_16x16x32_f16 v[50:53], v[178:181], v[154:157], v[50:53]
	v_mfma_f32_16x16x32_f16 v[46:49], v[154:157], v[182:185], v[46:49]
	v_mfma_f32_16x16x32_f16 v[140:143], v[154:157], v[186:189], v[2:5]
	v_mfma_f32_16x16x32_f16 v[38:41], v[166:169], v[158:161], v[38:41]
	v_mfma_f32_16x16x32_f16 v[66:69], v[170:173], v[158:161], v[66:69]
	v_mfma_f32_16x16x32_f16 v[78:81], v[174:177], v[158:161], v[78:81]
	v_mfma_f32_16x16x32_f16 v[82:85], v[178:181], v[158:161], v[82:85]
	v_mfma_f32_16x16x32_f16 v[90:93], v[158:161], v[182:185], v[90:93]
	v_mfma_f32_16x16x32_f16 v[94:97], v[158:161], v[186:189], v[94:97]
	v_mfma_f32_16x16x32_f16 v[22:25], v[166:169], v[162:165], v[22:25]
	v_mfma_f32_16x16x32_f16 v[102:105], v[170:173], v[162:165], v[102:105]
	v_mfma_f32_16x16x32_f16 v[30:33], v[174:177], v[162:165], v[30:33]
	v_mfma_f32_16x16x32_f16 v[26:29], v[178:181], v[162:165], v[26:29]
	v_mfma_f32_16x16x32_f16 v[34:37], v[162:165], v[182:185], v[34:37]
	v_mfma_f32_16x16x32_f16 v[152:155], v[162:165], v[186:189], v[6:9]
	s_waitcnt lgkmcnt(0)
	v_mfma_f32_16x16x32_f16 v[156:159], v[118:121], v[106:109], v[16:19]
	s_movk_i32 s0, 0x7c0
	ds_read_b128 v[202:205], v0 offset:9216
	ds_read_b128 v[206:209], v0 offset:11264
	v_lshlrev_b32_e32 v16, 6, v144
	v_mov_b32_e32 v17, 0
	v_mov_b32_e32 v139, v17
	v_lshl_add_u64 v[4:5], s[6:7], 0, v[16:17]
	v_lshl_add_u64 v[8:9], v[4:5], 0, v[138:139]
	s_waitcnt vmcnt(0)
	v_lshlrev_b32_e32 v4, 5, v150
	v_lshl_add_u64 v[2:3], s[4:5], 0, v[16:17]
	v_ashrrev_i32_e32 v5, 31, v4
	v_lshl_add_u64 v[2:3], v[2:3], 0, v[138:139]
	v_lshlrev_b64 v[4:5], 2, v[4:5]
	v_lshl_add_u64 v[6:7], v[2:3], 0, v[4:5]
	v_lshl_add_u64 v[4:5], v[8:9], 0, v[4:5]
	v_mfma_f32_16x16x32_f16 v[98:101], v[122:125], v[106:109], v[98:101]
	global_load_dwordx4 v[160:163], v[6:7], off
	v_lshlrev_b32_e32 v18, 5, v147
	v_ashrrev_i32_e32 v19, 31, v18
	v_mfma_f32_16x16x32_f16 v[86:89], v[126:129], v[106:109], v[86:89]
	v_lshlrev_b64 v[18:19], 2, v[18:19]
	ds_read_b128 v[172:175], v146 offset:62464
	ds_read_b128 v[176:179], v146 offset:64512
	v_mfma_f32_16x16x32_f16 v[74:77], v[130:133], v[106:109], v[74:77]
	v_mfma_f32_16x16x32_f16 v[70:73], v[106:109], v[134:137], v[70:73]
	v_mfma_f32_16x16x32_f16 v[42:45], v[106:109], v[190:193], v[42:45]
	global_load_dwordx4 v[106:109], v[4:5], off
	v_lshlrev_b32_e32 v4, 5, v149
	v_ashrrev_i32_e32 v5, 31, v4
	v_lshlrev_b64 v[4:5], 2, v[4:5]
	v_lshl_add_u64 v[6:7], v[2:3], 0, v[4:5]
	v_lshl_add_u64 v[4:5], v[8:9], 0, v[4:5]
	global_load_dwordx4 v[168:171], v[4:5], off
	global_load_dwordx4 v[164:167], v[6:7], off
	v_lshlrev_b32_e32 v4, 5, v148
	v_ashrrev_i32_e32 v5, 31, v4
	v_lshlrev_b64 v[10:11], 2, v[4:5]
	v_lshl_add_u64 v[4:5], v[2:3], 0, v[10:11]
	v_lshl_add_u64 v[10:11], v[8:9], 0, v[10:11]
	global_load_dwordx4 v[210:213], v[10:11], off
	v_lshl_add_u64 v[2:3], v[2:3], 0, v[18:19]
	global_load_dwordx4 v[4:7], v[4:5], off
	v_lshl_add_u64 v[8:9], v[8:9], 0, v[18:19]
	v_add_u32_e32 v18, 0x16400, v21
	v_ashrrev_i32_e32 v10, 7, v145
	ds_read_b128 v[180:183], v18
	v_add_u32_e32 v18, 0x17400, v21
	v_and_b32_e32 v10, -16, v10
	v_add_u32_e32 v19, 0x16c00, v21
	ds_read_b128 v[194:197], v18
	v_add_u32_e32 v18, s20, v10
	global_load_dwordx4 v[8:11], v[8:9], off
	ds_read_b128 v[184:187], v19
	v_add_u32_e32 v19, 0x17c00, v21
	v_and_or_b32 v21, v145, s0, v1
	global_load_dwordx4 v[0:3], v[2:3], off
	v_mfma_f32_16x16x32_f16 v[62:65], v[118:121], v[110:113], v[62:65]
	ds_read_b128 v[198:201], v19
	v_ashrrev_i32_e32 v19, 31, v18
	ds_read_b128 v[148:151], v146 offset:60416
	v_mfma_f32_16x16x32_f16 v[58:61], v[122:125], v[110:113], v[58:61]
	v_mfma_f32_16x16x32_f16 v[54:57], v[126:129], v[110:113], v[54:57]
	v_mfma_f32_16x16x32_f16 v[50:53], v[130:133], v[110:113], v[50:53]
	v_mfma_f32_16x16x32_f16 v[46:49], v[110:113], v[134:137], v[46:49]
	v_mfma_f32_16x16x32_f16 v[110:113], v[110:113], v[190:193], v[140:143]
	s_nop 2
	ds_read_b128 v[140:143], v146 offset:58368
	v_mfma_f32_16x16x32_f16 v[38:41], v[118:121], v[114:117], v[38:41]
	v_mfma_f32_16x16x32_f16 v[66:69], v[122:125], v[114:117], v[66:69]
	v_mfma_f32_16x16x32_f16 v[78:81], v[126:129], v[114:117], v[78:81]
	v_mfma_f32_16x16x32_f16 v[82:85], v[130:133], v[114:117], v[82:85]
	v_mfma_f32_16x16x32_f16 v[90:93], v[114:117], v[134:137], v[90:93]
	v_mfma_f32_16x16x32_f16 v[94:97], v[114:117], v[190:193], v[94:97]
	s_waitcnt lgkmcnt(0)
	v_mfma_f32_16x16x32_f16 v[114:117], v[180:183], v[140:143], v[156:159]
	v_mfma_f32_16x16x32_f16 v[98:101], v[184:187], v[140:143], v[98:101]
	v_mfma_f32_16x16x32_f16 v[22:25], v[118:121], v[12:15], v[22:25]
	s_waitcnt vmcnt(6)
	s_nop 4
	v_pk_mul_f32 v[120:121], v[114:115], v[106:107] op_sel_hi:[1,0]
	v_lshlrev_b64 v[118:119], 17, v[18:19]
	v_lshl_or_b32 v118, v21, 6, v118
	v_mfma_f32_16x16x32_f16 v[102:105], v[122:125], v[12:15], v[102:105]
	v_mul_f32_e64 v122, v116, v107
	v_mul_f32_e64 v123, v117, v107
	v_pk_fma_f32 v[124:125], v[114:115], v[160:161], v[120:121] op_sel:[0,0,1] op_sel_hi:[1,1,0] neg_lo:[0,0,1] neg_hi:[0,0,1]
	v_pk_fma_f32 v[114:115], v[114:115], v[160:161], v[120:121] op_sel:[0,0,1] op_sel_hi:[1,0,0]
	v_pk_fma_f32 v[120:121], v[116:117], v[160:161], v[122:123] op_sel:[0,1,1] op_sel_hi:[1,1,0] neg_lo:[0,0,1] neg_hi:[0,0,1]
	v_pk_fma_f32 v[116:117], v[116:117], v[160:161], v[122:123] op_sel:[0,1,1] op_sel_hi:[1,1,0]
	v_cvt_pk_f16_f32 v114, v124, v115
	v_cvt_pk_f16_f32 v115, v120, v117
	v_pk_mul_f32 v[116:117], v[98:99], v[108:109] op_sel_hi:[1,0]
	v_mov_b32_e32 v122, v163
	v_pk_fma_f32 v[120:121], v[98:99], v[162:163], v[116:117] op_sel:[0,0,1] op_sel_hi:[1,1,0] neg_lo:[0,0,1] neg_hi:[0,0,1]
	v_pk_fma_f32 v[98:99], v[98:99], v[162:163], v[116:117] op_sel:[0,0,1] op_sel_hi:[1,0,0]
	v_mfma_f32_16x16x32_f16 v[30:33], v[126:129], v[12:15], v[30:33]
	v_cvt_pk_f16_f32 v116, v120, v99
	v_mov_b32_e32 v120, v109
	v_pk_mul_f32 v[98:99], v[100:101], v[120:121] op_sel_hi:[1,0]
	v_mfma_f32_16x16x32_f16 v[26:29], v[130:133], v[12:15], v[26:29]
	v_fma_f32 v124, v100, v122, -v99
	v_fma_f32 v125, v101, v122, -v98
	v_pk_fma_f32 v[98:99], v[100:101], v[122:123], v[98:99] op_sel:[0,0,1] op_sel_hi:[1,0,0]
	s_nop 0
	v_cvt_pk_f16_f32 v117, v124, v99
	v_lshlrev_b64 v[124:125], 1, v[118:119]
	v_lshl_add_u64 v[126:127], s[10:11], 0, v[124:125]
	v_mfma_f32_16x16x32_f16 v[34:37], v[12:15], v[134:137], v[34:37]
	v_mfma_f32_16x16x32_f16 v[98:101], v[12:15], v[190:193], v[152:155]
	v_lshl_add_u64 v[12:13], v[126:127], 0, v[16:17]
	v_lshl_add_u64 v[126:127], v[12:13], 0, v[138:139]
	global_store_dwordx4 v[126:127], v[114:117], off sc1
	v_mfma_f32_16x16x32_f16 v[12:15], v[194:197], v[140:143], v[86:89]
	v_mfma_f32_16x16x32_f16 v[74:77], v[198:201], v[140:143], v[74:77]
	v_mfma_f32_16x16x32_f16 v[58:61], v[184:187], v[148:151], v[58:61]
	s_nop 5
	v_mul_f32_e64 v86, v12, v106
	v_mul_f32_e64 v87, v13, v106
	v_pk_fma_f32 v[88:89], v[12:13], v[160:161], v[86:87] op_sel:[0,0,1] op_sel_hi:[1,1,0] neg_lo:[0,0,1] neg_hi:[0,0,1]
	v_pk_fma_f32 v[12:13], v[12:13], v[160:161], v[86:87] op_sel:[0,0,1] op_sel_hi:[1,0,0]
	v_mfma_f32_16x16x32_f16 v[54:57], v[194:197], v[148:151], v[54:57]
	v_cvt_pk_f16_f32 v86, v88, v13
	v_pk_mul_f32 v[12:13], v[14:15], v[106:107] op_sel:[0,1]
	s_nop 0
	v_pk_fma_f32 v[88:89], v[14:15], v[160:161], v[12:13] op_sel:[0,1,1] op_sel_hi:[1,1,0] neg_lo:[0,0,1] neg_hi:[0,0,1]
	v_pk_fma_f32 v[12:13], v[14:15], v[160:161], v[12:13] op_sel:[0,1,1] op_sel_hi:[1,1,0]
	v_mfma_f32_16x16x32_f16 v[50:53], v[198:201], v[148:151], v[50:53]
	v_cvt_pk_f16_f32 v87, v88, v13
	v_pk_mul_f32 v[88:89], v[74:75], v[108:109] op_sel_hi:[1,0]
	v_mfma_f32_16x16x32_f16 v[12:15], v[140:143], v[206:209], v[42:45]
	s_nop 2
	v_fma_f32 v42, v74, v162, -v89
	v_fma_f32 v43, v75, v163, -v88
	v_pk_fma_f32 v[44:45], v[74:75], v[162:163], v[88:89] op_sel:[0,0,1] op_sel_hi:[1,0,0]
	v_mfma_f32_16x16x32_f16 v[38:41], v[180:183], v[172:175], v[38:41]
	v_cvt_pk_f16_f32 v88, v42, v45
	v_mfma_f32_16x16x32_f16 v[42:45], v[180:183], v[148:151], v[62:65]
	s_nop 2
	v_mul_f32_e64 v62, v76, v120
	v_mul_f32_e64 v63, v77, v120
	v_mfma_f32_16x16x32_f16 v[66:69], v[184:187], v[172:175], v[66:69]
	v_fma_f32 v64, v76, v122, -v63
	v_fma_f32 v65, v77, v122, -v62
	v_pk_fma_f32 v[62:63], v[76:77], v[122:123], v[62:63] op_sel:[0,0,1] op_sel_hi:[1,0,0]
	s_nop 0
	v_cvt_pk_f16_f32 v89, v64, v63
	v_lshl_add_u64 v[62:63], s[12:13], 0, v[124:125]
	v_lshl_add_u64 v[62:63], v[62:63], 0, v[16:17]
	v_lshl_add_u64 v[106:107], v[62:63], 0, v[138:139]
	s_waitcnt vmcnt(6)
	v_pk_mul_f32 v[62:63], v[42:43], v[168:169] op_sel_hi:[1,0]
	global_store_dwordx4 v[106:107], v[86:89], off sc1
	s_waitcnt vmcnt(6)
	v_pk_fma_f32 v[64:65], v[42:43], v[164:165], v[62:63] op_sel:[0,0,1] op_sel_hi:[1,1,0] neg_lo:[0,0,1] neg_hi:[0,0,1]
	v_pk_fma_f32 v[42:43], v[42:43], v[164:165], v[62:63] op_sel:[0,0,1] op_sel_hi:[1,0,0]
	v_pk_mul_f32 v[62:63], v[44:45], v[168:169] op_sel:[0,1]
	v_cvt_pk_f16_f32 v42, v64, v43
	v_pk_fma_f32 v[74:75], v[44:45], v[164:165], v[62:63] op_sel:[0,1,1] op_sel_hi:[1,1,0] neg_lo:[0,0,1] neg_hi:[0,0,1]
	v_pk_fma_f32 v[44:45], v[44:45], v[164:165], v[62:63] op_sel:[0,1,1] op_sel_hi:[1,1,0]
	v_mov_b32_e32 v86, v171
	v_cvt_pk_f16_f32 v43, v74, v45
	v_pk_mul_f32 v[44:45], v[58:59], v[170:171] op_sel_hi:[1,0]
	v_mov_b32_e32 v88, v167
	v_pk_fma_f32 v[74:75], v[58:59], v[166:167], v[44:45] op_sel:[0,0,1] op_sel_hi:[1,1,0] neg_lo:[0,0,1] neg_hi:[0,0,1]
	v_pk_fma_f32 v[44:45], v[58:59], v[166:167], v[44:45] op_sel:[0,0,1] op_sel_hi:[1,0,0]
	v_pk_mul_f32 v[58:59], v[60:61], v[86:87] op_sel_hi:[1,0]
	v_cvt_pk_f16_f32 v44, v74, v45
	v_pk_fma_f32 v[108:109], v[60:61], v[88:89], v[58:59] op_sel:[0,0,1] op_sel_hi:[1,0,0] neg_lo:[0,0,1] neg_hi:[0,0,1]
	v_pk_fma_f32 v[58:59], v[60:61], v[88:89], v[58:59] op_sel:[0,0,1] op_sel_hi:[1,0,0]
	v_mfma_f32_16x16x32_f16 v[74:77], v[194:197], v[172:175], v[78:81]
	v_cvt_pk_f16_f32 v45, v108, v59
	global_store_dwordx4 v[126:127], v[42:45], off offset:2048 sc1
	v_pk_mul_f32 v[58:59], v[54:55], v[168:169] op_sel_hi:[1,0]
	v_mfma_f32_16x16x32_f16 v[22:25], v[180:183], v[176:179], v[22:25]
	v_fma_f32 v78, v54, v164, -v59
	v_fma_f32 v79, v55, v165, -v58
	v_pk_fma_f32 v[54:55], v[54:55], v[164:165], v[58:59] op_sel:[0,0,1] op_sel_hi:[1,0,0]
	v_mfma_f32_16x16x32_f16 v[42:45], v[198:201], v[172:175], v[82:85]
	v_cvt_pk_f16_f32 v54, v78, v55
	s_nop 1
	v_pk_mul_f32 v[82:83], v[56:57], v[168:169] op_sel:[0,1]
	v_mfma_f32_16x16x32_f16 v[30:33], v[194:197], v[176:179], v[30:33]
	v_fma_f32 v84, v56, v165, -v83
	v_fma_f32 v85, v57, v165, -v82
	v_pk_fma_f32 v[56:57], v[56:57], v[164:165], v[82:83] op_sel:[0,1,1] op_sel_hi:[1,1,0]
	s_nop 0
	v_cvt_pk_f16_f32 v55, v84, v57
	v_pk_mul_f32 v[56:57], v[50:51], v[170:171] op_sel_hi:[1,0]
	v_mfma_f32_16x16x32_f16 v[26:29], v[198:201], v[176:179], v[26:29]
	v_fma_f32 v82, v50, v166, -v57
	v_fma_f32 v83, v51, v167, -v56
	v_pk_fma_f32 v[50:51], v[50:51], v[166:167], v[56:57] op_sel:[0,0,1] op_sel_hi:[1,0,0]
	s_nop 0
	v_cvt_pk_f16_f32 v56, v82, v51
	v_pk_mul_f32 v[50:51], v[52:53], v[86:87] op_sel_hi:[1,0]
	v_mfma_f32_16x16x32_f16 v[82:85], v[184:187], v[176:179], v[102:105]
	v_fma_f32 v86, v52, v88, -v51
	v_fma_f32 v87, v53, v88, -v50
	v_pk_fma_f32 v[50:51], v[52:53], v[88:89], v[50:51] op_sel:[0,0,1] op_sel_hi:[1,0,0]
	s_nop 0
	v_cvt_pk_f16_f32 v57, v86, v51
	global_store_dwordx4 v[106:107], v[54:57], off offset:2048 sc1
	s_waitcnt vmcnt(7)
	v_pk_mul_f32 v[50:51], v[38:39], v[210:211] op_sel_hi:[1,0]
	v_mfma_f32_16x16x32_f16 v[70:73], v[140:143], v[202:205], v[70:73]
	v_mul_f32_e64 v56, v40, v211
	v_mul_f32_e64 v57, v41, v211
	s_waitcnt vmcnt(6)
	v_pk_fma_f32 v[52:53], v[38:39], v[4:5], v[50:51] op_sel:[0,0,1] op_sel_hi:[1,1,0] neg_lo:[0,0,1] neg_hi:[0,0,1]
	v_pk_fma_f32 v[38:39], v[38:39], v[4:5], v[50:51] op_sel:[0,0,1] op_sel_hi:[1,0,0]
	v_pk_fma_f32 v[86:87], v[40:41], v[4:5], v[56:57] op_sel:[0,1,1] op_sel_hi:[1,1,0] neg_lo:[0,0,1] neg_hi:[0,0,1]
	v_pk_fma_f32 v[40:41], v[40:41], v[4:5], v[56:57] op_sel:[0,1,1] op_sel_hi:[1,1,0]
	v_cvt_pk_f16_f32 v38, v52, v39
	v_cvt_pk_f16_f32 v39, v86, v41
	v_pk_mul_f32 v[40:41], v[66:67], v[212:213] op_sel_hi:[1,0]
	v_or_b32_e32 v54, 0x800, v118
	v_pk_fma_f32 v[56:57], v[66:67], v[6:7], v[40:41] op_sel:[0,0,1] op_sel_hi:[1,1,0] neg_lo:[0,0,1] neg_hi:[0,0,1]
	v_pk_fma_f32 v[40:41], v[66:67], v[6:7], v[40:41] op_sel:[0,0,1] op_sel_hi:[1,0,0]
	v_mov_b32_e32 v55, v119
	v_cvt_pk_f16_f32 v40, v56, v41
	v_mov_b32_e32 v56, v213
	v_pk_mul_f32 v[66:67], v[68:69], v[56:57] op_sel_hi:[1,0]
	v_mov_b32_e32 v86, v7
	v_pk_fma_f32 v[88:89], v[68:69], v[86:87], v[66:67] op_sel:[0,0,1] op_sel_hi:[1,0,0] neg_lo:[0,0,1] neg_hi:[0,0,1]
	v_pk_fma_f32 v[66:67], v[68:69], v[86:87], v[66:67] op_sel:[0,0,1] op_sel_hi:[1,0,0]
	v_lshlrev_b64 v[54:55], 1, v[54:55]
	v_cvt_pk_f16_f32 v41, v88, v67
	v_lshl_add_u64 v[66:67], s[10:11], 0, v[54:55]
	v_lshl_add_u64 v[66:67], v[66:67], 0, v[16:17]
	v_lshl_add_u64 v[66:67], v[66:67], 0, v[138:139]
	global_store_dwordx4 v[66:67], v[38:41], off sc1
	v_or_b32_e32 v118, 0xc00, v118
	v_mfma_f32_16x16x32_f16 v[46:49], v[148:151], v[202:205], v[46:49]
	v_mul_f32_e64 v38, v74, v210
	v_mul_f32_e64 v39, v75, v210
	v_pk_fma_f32 v[40:41], v[74:75], v[4:5], v[38:39] op_sel:[0,0,1] op_sel_hi:[1,1,0] neg_lo:[0,0,1] neg_hi:[0,0,1]
	v_pk_fma_f32 v[38:39], v[74:75], v[4:5], v[38:39] op_sel:[0,0,1] op_sel_hi:[1,0,0]
	v_mfma_f32_16x16x32_f16 v[58:61], v[172:175], v[202:205], v[90:93]
	v_cvt_pk_f16_f32 v38, v40, v39
	v_pk_mul_f32 v[40:41], v[76:77], v[210:211] op_sel:[0,1]
	s_nop 0
	v_pk_fma_f32 v[66:67], v[76:77], v[4:5], v[40:41] op_sel:[0,1,1] op_sel_hi:[1,1,0] neg_lo:[0,0,1] neg_hi:[0,0,1]
	v_pk_fma_f32 v[4:5], v[76:77], v[4:5], v[40:41] op_sel:[0,1,1] op_sel_hi:[1,1,0]
	v_mfma_f32_16x16x32_f16 v[34:37], v[176:179], v[202:205], v[34:37]
	v_cvt_pk_f16_f32 v39, v66, v5
	v_pk_mul_f32 v[4:5], v[42:43], v[212:213] op_sel_hi:[1,0]
	s_nop 0
	v_pk_fma_f32 v[40:41], v[42:43], v[6:7], v[4:5] op_sel:[0,0,1] op_sel_hi:[1,1,0] neg_lo:[0,0,1] neg_hi:[0,0,1]
	v_pk_fma_f32 v[4:5], v[42:43], v[6:7], v[4:5] op_sel:[0,0,1] op_sel_hi:[1,0,0]
	v_mfma_f32_16x16x32_f16 v[62:65], v[148:151], v[206:209], v[110:113]
	v_cvt_pk_f16_f32 v40, v40, v5
	v_pk_mul_f32 v[4:5], v[44:45], v[56:57] op_sel_hi:[1,0]
	s_nop 0
	v_pk_fma_f32 v[6:7], v[44:45], v[86:87], v[4:5] op_sel:[0,0,1] op_sel_hi:[1,0,0] neg_lo:[0,0,1] neg_hi:[0,0,1]
	v_pk_fma_f32 v[4:5], v[44:45], v[86:87], v[4:5] op_sel:[0,0,1] op_sel_hi:[1,0,0]
	v_mfma_f32_16x16x32_f16 v[78:81], v[172:175], v[206:209], v[94:97]
	v_cvt_pk_f16_f32 v41, v6, v5
	v_lshl_add_u64 v[4:5], s[12:13], 0, v[54:55]
	v_lshl_add_u64 v[4:5], v[4:5], 0, v[16:17]
	v_lshl_add_u64 v[4:5], v[4:5], 0, v[138:139]
	global_store_dwordx4 v[4:5], v[38:41], off sc1
	s_waitcnt vmcnt(7)
	v_pk_mul_f32 v[4:5], v[22:23], v[8:9] op_sel_hi:[1,0]
	v_mfma_f32_16x16x32_f16 v[50:53], v[176:179], v[206:209], v[98:101]
	s_waitcnt vmcnt(6)
	v_pk_fma_f32 v[6:7], v[22:23], v[0:1], v[4:5] op_sel:[0,0,1] op_sel_hi:[1,1,0] neg_lo:[0,0,1] neg_hi:[0,0,1]
	v_pk_fma_f32 v[4:5], v[22:23], v[0:1], v[4:5] op_sel:[0,0,1] op_sel_hi:[1,0,0]
	v_mov_b32_e32 v38, v3
	v_cvt_pk_f16_f32 v4, v6, v5
	v_pk_mul_f32 v[6:7], v[24:25], v[8:9] op_sel:[0,1]
	s_nop 0
	v_pk_fma_f32 v[22:23], v[24:25], v[0:1], v[6:7] op_sel:[0,1,1] op_sel_hi:[1,1,0] neg_lo:[0,0,1] neg_hi:[0,0,1]
	v_pk_fma_f32 v[6:7], v[24:25], v[0:1], v[6:7] op_sel:[0,1,1] op_sel_hi:[1,1,0]
	s_nop 0
	v_cvt_pk_f16_f32 v5, v22, v7
	v_pk_mul_f32 v[6:7], v[82:83], v[10:11] op_sel_hi:[1,0]
	s_nop 0
	v_pk_fma_f32 v[22:23], v[82:83], v[2:3], v[6:7] op_sel:[0,0,1] op_sel_hi:[1,1,0] neg_lo:[0,0,1] neg_hi:[0,0,1]
	v_pk_fma_f32 v[6:7], v[82:83], v[2:3], v[6:7] op_sel:[0,0,1] op_sel_hi:[1,0,0]
	s_nop 0
	v_cvt_pk_f16_f32 v6, v22, v7
	v_mov_b32_e32 v22, v11
	v_pk_mul_f32 v[24:25], v[84:85], v[22:23] op_sel_hi:[1,0]
	s_nop 0
	v_pk_fma_f32 v[40:41], v[84:85], v[38:39], v[24:25] op_sel:[0,0,1] op_sel_hi:[1,0,0] neg_lo:[0,0,1] neg_hi:[0,0,1]
	v_pk_fma_f32 v[24:25], v[84:85], v[38:39], v[24:25] op_sel:[0,0,1] op_sel_hi:[1,0,0]
	s_nop 0
	v_cvt_pk_f16_f32 v7, v40, v25
	v_lshlrev_b64 v[24:25], 1, v[118:119]
	v_lshl_add_u64 v[40:41], s[10:11], 0, v[24:25]
	v_lshl_add_u64 v[40:41], v[40:41], 0, v[16:17]
	v_lshl_add_u64 v[40:41], v[40:41], 0, v[138:139]
	global_store_dwordx4 v[40:41], v[4:7], off sc1
	s_nop 1
	v_pk_mul_f32 v[4:5], v[30:31], v[8:9] op_sel_hi:[1,0]
	s_nop 0
	v_pk_fma_f32 v[6:7], v[30:31], v[0:1], v[4:5] op_sel:[0,0,1] op_sel_hi:[1,1,0] neg_lo:[0,0,1] neg_hi:[0,0,1]
	v_pk_fma_f32 v[4:5], v[30:31], v[0:1], v[4:5] op_sel:[0,0,1] op_sel_hi:[1,0,0]
	s_nop 0
	v_cvt_pk_f16_f32 v4, v6, v5
	v_pk_mul_f32 v[6:7], v[32:33], v[8:9] op_sel:[0,1]
	s_nop 0
	v_pk_fma_f32 v[8:9], v[32:33], v[0:1], v[6:7] op_sel:[0,1,1] op_sel_hi:[1,1,0] neg_lo:[0,0,1] neg_hi:[0,0,1]
	v_pk_fma_f32 v[0:1], v[32:33], v[0:1], v[6:7] op_sel:[0,1,1] op_sel_hi:[1,1,0]
	s_nop 0
	v_cvt_pk_f16_f32 v5, v8, v1
	v_pk_mul_f32 v[0:1], v[26:27], v[10:11] op_sel_hi:[1,0]
	s_nop 0
	v_pk_fma_f32 v[6:7], v[26:27], v[2:3], v[0:1] op_sel:[0,0,1] op_sel_hi:[1,1,0] neg_lo:[0,0,1] neg_hi:[0,0,1]
	v_pk_fma_f32 v[0:1], v[26:27], v[2:3], v[0:1] op_sel:[0,0,1] op_sel_hi:[1,0,0]
	s_nop 0
	v_cvt_pk_f16_f32 v6, v6, v1
	v_pk_mul_f32 v[0:1], v[28:29], v[22:23] op_sel_hi:[1,0]
	s_nop 0
	v_pk_fma_f32 v[2:3], v[28:29], v[38:39], v[0:1] op_sel:[0,0,1] op_sel_hi:[1,0,0] neg_lo:[0,0,1] neg_hi:[0,0,1]
	v_pk_fma_f32 v[0:1], v[28:29], v[38:39], v[0:1] op_sel:[0,0,1] op_sel_hi:[1,0,0]
	v_cvt_pk_f16_f32 v3, v48, v49
	v_cvt_pk_f16_f32 v7, v2, v1
	v_lshl_add_u64 v[0:1], s[12:13], 0, v[24:25]
	v_lshl_add_u64 v[0:1], v[0:1], 0, v[16:17]
	v_lshl_add_u64 v[0:1], v[0:1], 0, v[138:139]
	global_store_dwordx4 v[0:1], v[4:7], off sc1
	v_lshlrev_b64 v[0:1], 18, v[18:19]
	v_lshlrev_b32_e32 v2, 7, v145
	v_lshl_add_u64 v[0:1], s[14:15], 0, v[0:1]
	v_and_b32_e32 v16, 0x3e000, v2
	v_lshl_add_u64 v[0:1], v[0:1], 0, v[16:17]
	v_lshlrev_b32_e32 v16, 4, v20
	v_lshl_add_u64 v[4:5], v[0:1], 0, v[16:17]
	v_lshlrev_b32_e32 v16, 12, v144
	v_cvt_pk_f16_f32 v2, v46, v47
	v_cvt_pk_f16_f32 v1, v72, v73
	v_cvt_pk_f16_f32 v0, v70, v71
	v_lshl_add_u64 v[4:5], v[4:5], 0, v[16:17]
	global_store_dwordx4 v[4:5], v[0:3], off sc1
	s_nop 1
	v_cvt_pk_f16_f32 v3, v36, v37
	v_cvt_pk_f16_f32 v2, v34, v35
	v_cvt_pk_f16_f32 v1, v60, v61
	v_cvt_pk_f16_f32 v0, v58, v59
	global_store_dwordx4 v[4:5], v[0:3], off offset:1024 sc1
	s_nop 1
	v_cvt_pk_f16_f32 v3, v64, v65
	v_cvt_pk_f16_f32 v2, v62, v63
	v_cvt_pk_f16_f32 v1, v14, v15
	v_cvt_pk_f16_f32 v0, v12, v13
	global_store_dwordx4 v[4:5], v[0:3], off offset:2048 sc1
	s_nop 1
	v_cvt_pk_f16_f32 v3, v52, v53
	v_cvt_pk_f16_f32 v2, v50, v51
	v_cvt_pk_f16_f32 v1, v80, v81
	v_cvt_pk_f16_f32 v0, v78, v79
	global_store_dwordx4 v[4:5], v[0:3], off offset:3072 sc1
	s_endpgm
	.p2align	8
